# speedup vs baseline: 1.0155x; 1.0019x over previous
.LBB1_76:
	s_or_b64 exec, exec, s[8:9]
	v_mbcnt_lo_u32_b32 v2, -1, 0
	v_mbcnt_hi_u32_b32 v2, -1, v2
	v_lshrrev_b32_e32 v42, 5, v68
	v_and_b32_e32 v67, 64, v2
	v_lshlrev_b32_e32 v2, 2, v0
	v_and_b32_e32 v43, 0x7c, v2
	v_or_b32_e32 v2, v67, v42
	v_lshlrev_b32_e32 v69, 2, v2
	s_waitcnt vmcnt(0)
	ds_bpermute_b32 v2, v69, v66
	ds_bpermute_b32 v6, v69, v66 offset:8
	ds_bpermute_b32 v10, v69, v66 offset:16
	ds_bpermute_b32 v14, v69, v66 offset:24
	v_lshlrev_b32_e32 v64, 2, v43
	v_mov_b32_e32 v65, 0
	ds_bpermute_b32 v18, v69, v66 offset:32
	s_waitcnt lgkmcnt(0)
	v_lshl_add_u64 v[40:41], s[4:5], 0, v[64:65]
	v_max_i32_e32 v64, 0, v2
	ds_bpermute_b32 v22, v69, v66 offset:40
	v_lshlrev_b64 v[2:3], 9, v[64:65]
	v_max_i32_e32 v64, 0, v6
	ds_bpermute_b32 v26, v69, v66 offset:48
	v_lshlrev_b64 v[6:7], 9, v[64:65]
	v_max_i32_e32 v64, 0, v10
	ds_bpermute_b32 v30, v69, v66 offset:56
	v_lshlrev_b64 v[10:11], 9, v[64:65]
	v_max_i32_e32 v64, 0, v14
	ds_bpermute_b32 v34, v69, v66 offset:64
	v_lshlrev_b64 v[14:15], 9, v[64:65]
	v_max_i32_e32 v64, 0, v18
	ds_bpermute_b32 v44, v69, v66 offset:72
	v_lshlrev_b64 v[18:19], 9, v[64:65]
	s_waitcnt lgkmcnt(4)
	v_max_i32_e32 v64, 0, v22
	ds_bpermute_b32 v48, v69, v66 offset:80
	v_lshlrev_b64 v[22:23], 9, v[64:65]
	s_waitcnt lgkmcnt(4)
	v_max_i32_e32 v64, 0, v26
	ds_bpermute_b32 v52, v69, v66 offset:88
	v_lshlrev_b64 v[26:27], 9, v[64:65]
	s_waitcnt lgkmcnt(4)
	v_max_i32_e32 v64, 0, v30
	ds_bpermute_b32 v56, v69, v66 offset:96
	v_lshlrev_b64 v[30:31], 9, v[64:65]
	s_waitcnt lgkmcnt(4)
	v_max_i32_e32 v64, 0, v34
	ds_bpermute_b32 v60, v69, v66 offset:104
	v_lshlrev_b64 v[34:35], 9, v[64:65]
	s_waitcnt lgkmcnt(4)
	v_max_i32_e32 v64, 0, v44
	ds_bpermute_b32 v70, v69, v66 offset:112
	v_lshl_add_u64 v[2:3], v[40:41], 0, v[2:3]
	v_lshl_add_u64 v[6:7], v[40:41], 0, v[6:7]
	v_lshlrev_b64 v[44:45], 9, v[64:65]
	s_waitcnt lgkmcnt(4)
	v_max_i32_e32 v64, 0, v48
	ds_bpermute_b32 v69, v69, v66 offset:120
	global_load_dwordx4 v[2:5], v[2:3], off nt
	v_lshl_add_u64 v[10:11], v[40:41], 0, v[10:11]
	global_load_dwordx4 v[6:9], v[6:7], off nt
	v_lshl_add_u64 v[14:15], v[40:41], 0, v[14:15]
	v_lshlrev_b64 v[48:49], 9, v[64:65]
	s_waitcnt lgkmcnt(4)
	v_max_i32_e32 v64, 0, v52
	global_load_dwordx4 v[10:13], v[10:11], off nt
	v_lshl_add_u64 v[18:19], v[40:41], 0, v[18:19]
	global_load_dwordx4 v[14:17], v[14:15], off nt
	v_lshl_add_u64 v[22:23], v[40:41], 0, v[22:23]
	v_lshlrev_b64 v[52:53], 9, v[64:65]
	s_waitcnt lgkmcnt(3)
	v_max_i32_e32 v64, 0, v56
	global_load_dwordx4 v[18:21], v[18:19], off nt
	v_lshl_add_u64 v[26:27], v[40:41], 0, v[26:27]
	global_load_dwordx4 v[22:25], v[22:23], off nt
	v_lshl_add_u64 v[30:31], v[40:41], 0, v[30:31]
	v_lshlrev_b64 v[56:57], 9, v[64:65]
	s_waitcnt lgkmcnt(2)
	v_max_i32_e32 v64, 0, v60
	global_load_dwordx4 v[26:29], v[26:27], off nt
	v_lshl_add_u64 v[34:35], v[40:41], 0, v[34:35]
	global_load_dwordx4 v[30:33], v[30:31], off nt
	v_lshl_add_u64 v[44:45], v[40:41], 0, v[44:45]
	v_lshlrev_b64 v[60:61], 9, v[64:65]
	s_waitcnt lgkmcnt(1)
	v_max_i32_e32 v64, 0, v70
	global_load_dwordx4 v[34:37], v[34:35], off nt
	v_lshl_add_u64 v[48:49], v[40:41], 0, v[48:49]
	global_load_dwordx4 v[44:47], v[44:45], off nt
	v_lshl_add_u64 v[52:53], v[40:41], 0, v[52:53]
	v_lshlrev_b64 v[70:71], 9, v[64:65]
	s_waitcnt lgkmcnt(0)
	v_max_i32_e32 v64, 0, v69
	global_load_dwordx4 v[48:51], v[48:49], off nt
	v_lshl_add_u64 v[56:57], v[40:41], 0, v[56:57]
	global_load_dwordx4 v[52:55], v[52:53], off nt
	v_lshl_add_u64 v[60:61], v[40:41], 0, v[60:61]
	v_lshlrev_b64 v[74:75], 9, v[64:65]
	global_load_dwordx4 v[56:59], v[56:57], off nt
	v_lshl_add_u64 v[70:71], v[40:41], 0, v[70:71]
	global_load_dwordx4 v[60:63], v[60:61], off nt
	v_lshl_add_u64 v[40:41], v[40:41], 0, v[74:75]
	global_load_dwordx4 v[70:73], v[70:71], off nt
	v_mul_u32_u24_e32 v69, 0x2200, v1
	global_load_dwordx4 v[74:77], v[40:41], off nt
	s_add_u32 s16, s6, s14
	s_addc_u32 s17, s7, 0
	s_add_u32 s18, s16, 0x1000
	s_addc_u32 s19, s17, 0
	s_add_u32 s20, s16, 0x2000
	s_addc_u32 s21, s17, 0
	s_add_u32 s22, s16, 0x3000
	s_addc_u32 s23, s17, 0
	s_add_u32 s24, s16, 0x4000
	s_addc_u32 s25, s17, 0
	s_add_u32 s26, s16, 0x5000
	s_addc_u32 s27, s17, 0
	s_add_u32 s28, s16, 0x6000
	s_addc_u32 s29, s17, 0
	s_add_u32 s30, s16, 0x7000
	s_addc_u32 s31, s17, 0
	v_and_b32_e32 v116, 63, v0
	v_lshlrev_b32_e32 v116, 4, v116
	global_load_dwordx4 v[84:87], v116, s[16:17]
	global_load_dwordx4 v[88:91], v116, s[18:19]
	global_load_dwordx4 v[92:95], v116, s[20:21]
	global_load_dwordx4 v[96:99], v116, s[22:23]
	global_load_dwordx4 v[100:103], v116, s[24:25]
	global_load_dwordx4 v[104:107], v116, s[26:27]
	global_load_dwordx4 v[108:111], v116, s[28:29]
	global_load_dwordx4 v[112:115], v116, s[30:31]
	v_lshl_or_b32 v40, v43, 1, v69
	s_movk_i32 s4, 0x110
	v_mad_u32_u24 v40, v42, s4, v40
	v_lshlrev_b32_e32 v64, 4, v68
	s_movk_i32 s0, 0x2200
	v_lshrrev_b32_e32 v68, 4, v68
	s_waitcnt vmcnt(23)
	v_cvt_pk_f16_f32 v5, v4, v5
	v_cvt_pk_f16_f32 v4, v2, v3
	s_waitcnt vmcnt(22)
	v_cvt_pk_f16_f32 v3, v8, v9
	v_cvt_pk_f16_f32 v2, v6, v7
	ds_write2_b64 v40, v[4:5], v[2:3] offset1:68
	v_add_u32_e32 v6, 0x800, v40
	s_waitcnt vmcnt(21)
	v_cvt_pk_f16_f32 v3, v12, v13
	v_cvt_pk_f16_f32 v2, v10, v11
	s_waitcnt vmcnt(20)
	v_cvt_pk_f16_f32 v5, v16, v17
	v_cvt_pk_f16_f32 v4, v14, v15
	ds_write2_b64 v40, v[2:3], v[4:5] offset0:136 offset1:204
	s_waitcnt vmcnt(19)
	v_cvt_pk_f16_f32 v3, v20, v21
	v_cvt_pk_f16_f32 v2, v18, v19
	s_waitcnt vmcnt(18)
	v_cvt_pk_f16_f32 v5, v24, v25
	v_cvt_pk_f16_f32 v4, v22, v23
	ds_write2_b64 v6, v[2:3], v[4:5] offset0:16 offset1:84
	s_waitcnt vmcnt(17)
	v_cvt_pk_f16_f32 v3, v28, v29
	v_cvt_pk_f16_f32 v2, v26, v27
	s_waitcnt vmcnt(16)
	v_cvt_pk_f16_f32 v5, v32, v33
	v_cvt_pk_f16_f32 v4, v30, v31
	ds_write2_b64 v6, v[2:3], v[4:5] offset0:152 offset1:220
	v_add_u32_e32 v6, 0x1000, v40
	s_waitcnt vmcnt(15)
	v_cvt_pk_f16_f32 v3, v36, v37
	v_cvt_pk_f16_f32 v2, v34, v35
	s_waitcnt vmcnt(14)
	v_cvt_pk_f16_f32 v5, v46, v47
	v_cvt_pk_f16_f32 v4, v44, v45
	ds_write2_b64 v6, v[2:3], v[4:5] offset0:32 offset1:100
	s_waitcnt vmcnt(13)
	v_cvt_pk_f16_f32 v3, v50, v51
	v_cvt_pk_f16_f32 v2, v48, v49
	s_waitcnt vmcnt(12)
	v_cvt_pk_f16_f32 v5, v54, v55
	v_cvt_pk_f16_f32 v4, v52, v53
	ds_write2_b64 v6, v[2:3], v[4:5] offset0:168 offset1:236
	s_waitcnt vmcnt(11)
	v_cvt_pk_f16_f32 v3, v58, v59
	v_cvt_pk_f16_f32 v2, v56, v57
	s_waitcnt vmcnt(10)
	v_cvt_pk_f16_f32 v5, v62, v63
	v_cvt_pk_f16_f32 v4, v60, v61
	v_add_u32_e32 v6, 0x1800, v40
	ds_write2_b64 v6, v[2:3], v[4:5] offset0:48 offset1:116
	s_waitcnt vmcnt(9)
	v_cvt_pk_f16_f32 v3, v72, v73
	v_cvt_pk_f16_f32 v2, v70, v71
	s_waitcnt vmcnt(8)
	v_cvt_pk_f16_f32 v5, v76, v77
	v_cvt_pk_f16_f32 v4, v74, v75
	ds_write2_b64 v6, v[2:3], v[4:5] offset0:184 offset1:252
	v_lshrrev_b32_e32 v118, 6, v0
	s_movk_i32 s33, 0x110
	v_mul_u32_u24_e32 v117, 0x2200, v118
	v_and_b32_e32 v118, 15, v0
	v_bfe_u32 v119, v0, 4, 2
	v_lshlrev_b32_e32 v67, 4, v118
	v_mad_u32_u24 v121, v119, s33, v117
	v_add_u32_e32 v121, v121, v67
	v_mad_u32_u24 v117, v118, s33, v117
	v_lshl_add_u32 v120, v119, 3, v117
	v_lshl_add_u32 v117, v119, 4, v117
	v_lshlrev_b32_e32 v119, 2, v119
	ds_read_b128 v[68:71], v117
	ds_read_b128 v[72:75], v117 offset:4352
	ds_read_b128 v[76:79], v117 offset:64
	ds_read_b128 v[80:83], v117 offset:4416
	s_waitcnt lgkmcnt(2)
	s_waitcnt vmcnt(7)
	v_mfma_f32_16x16x32_f16 v[2:5], v[84:87], v[68:71], 0
	v_mfma_f32_16x16x32_f16 v[34:37], v[84:87], v[72:75], 0
	global_load_dwordx4 v[84:87], v116, s[16:17] offset:1024
	s_waitcnt vmcnt(7)
	v_mfma_f32_16x16x32_f16 v[6:9], v[88:91], v[68:71], 0
	v_mfma_f32_16x16x32_f16 v[38:41], v[88:91], v[72:75], 0
	global_load_dwordx4 v[88:91], v116, s[18:19] offset:1024
	s_waitcnt vmcnt(7)
	v_mfma_f32_16x16x32_f16 v[10:13], v[92:95], v[68:71], 0
	v_mfma_f32_16x16x32_f16 v[42:45], v[92:95], v[72:75], 0
	global_load_dwordx4 v[92:95], v116, s[20:21] offset:1024
	s_waitcnt vmcnt(7)
	v_mfma_f32_16x16x32_f16 v[14:17], v[96:99], v[68:71], 0
	v_mfma_f32_16x16x32_f16 v[46:49], v[96:99], v[72:75], 0
	global_load_dwordx4 v[96:99], v116, s[22:23] offset:1024
	s_waitcnt vmcnt(7)
	v_mfma_f32_16x16x32_f16 v[18:21], v[100:103], v[68:71], 0
	v_mfma_f32_16x16x32_f16 v[50:53], v[100:103], v[72:75], 0
	global_load_dwordx4 v[100:103], v116, s[24:25] offset:1024
	s_waitcnt vmcnt(7)
	v_mfma_f32_16x16x32_f16 v[22:25], v[104:107], v[68:71], 0
	v_mfma_f32_16x16x32_f16 v[54:57], v[104:107], v[72:75], 0
	global_load_dwordx4 v[104:107], v116, s[26:27] offset:1024
	s_waitcnt vmcnt(7)
	v_mfma_f32_16x16x32_f16 v[26:29], v[108:111], v[68:71], 0
	v_mfma_f32_16x16x32_f16 v[58:61], v[108:111], v[72:75], 0
	global_load_dwordx4 v[108:111], v116, s[28:29] offset:1024
	s_waitcnt vmcnt(7)
	v_mfma_f32_16x16x32_f16 v[30:33], v[112:115], v[68:71], 0
	v_mfma_f32_16x16x32_f16 v[62:65], v[112:115], v[72:75], 0
	global_load_dwordx4 v[112:115], v116, s[30:31] offset:1024
	ds_read_b128 v[68:71], v117 offset:128
	ds_read_b128 v[72:75], v117 offset:4480
	s_waitcnt lgkmcnt(2)
	s_waitcnt vmcnt(7)
	v_mfma_f32_16x16x32_f16 v[2:5], v[84:87], v[76:79], v[2:5]
	v_mfma_f32_16x16x32_f16 v[34:37], v[84:87], v[80:83], v[34:37]
	global_load_dwordx4 v[84:87], v116, s[16:17] offset:2048
	s_waitcnt vmcnt(7)
	v_mfma_f32_16x16x32_f16 v[6:9], v[88:91], v[76:79], v[6:9]
	v_mfma_f32_16x16x32_f16 v[38:41], v[88:91], v[80:83], v[38:41]
	global_load_dwordx4 v[88:91], v116, s[18:19] offset:2048
	s_waitcnt vmcnt(7)
	v_mfma_f32_16x16x32_f16 v[10:13], v[92:95], v[76:79], v[10:13]
	v_mfma_f32_16x16x32_f16 v[42:45], v[92:95], v[80:83], v[42:45]
	global_load_dwordx4 v[92:95], v116, s[20:21] offset:2048
	s_waitcnt vmcnt(7)
	v_mfma_f32_16x16x32_f16 v[14:17], v[96:99], v[76:79], v[14:17]
	v_mfma_f32_16x16x32_f16 v[46:49], v[96:99], v[80:83], v[46:49]
	global_load_dwordx4 v[96:99], v116, s[22:23] offset:2048
	s_waitcnt vmcnt(7)
	v_mfma_f32_16x16x32_f16 v[18:21], v[100:103], v[76:79], v[18:21]
	v_mfma_f32_16x16x32_f16 v[50:53], v[100:103], v[80:83], v[50:53]
	global_load_dwordx4 v[100:103], v116, s[24:25] offset:2048
	s_waitcnt vmcnt(7)
	v_mfma_f32_16x16x32_f16 v[22:25], v[104:107], v[76:79], v[22:25]
	v_mfma_f32_16x16x32_f16 v[54:57], v[104:107], v[80:83], v[54:57]
	global_load_dwordx4 v[104:107], v116, s[26:27] offset:2048
	s_waitcnt vmcnt(7)
	v_mfma_f32_16x16x32_f16 v[26:29], v[108:111], v[76:79], v[26:29]
	v_mfma_f32_16x16x32_f16 v[58:61], v[108:111], v[80:83], v[58:61]
	global_load_dwordx4 v[108:111], v116, s[28:29] offset:2048
	s_waitcnt vmcnt(7)
	v_mfma_f32_16x16x32_f16 v[30:33], v[112:115], v[76:79], v[30:33]
	v_mfma_f32_16x16x32_f16 v[62:65], v[112:115], v[80:83], v[62:65]
	global_load_dwordx4 v[112:115], v116, s[30:31] offset:2048
	ds_read_b128 v[76:79], v117 offset:192
	ds_read_b128 v[80:83], v117 offset:4544
	s_waitcnt lgkmcnt(2)
	s_waitcnt vmcnt(7)
	v_mfma_f32_16x16x32_f16 v[2:5], v[84:87], v[68:71], v[2:5]
	v_mfma_f32_16x16x32_f16 v[34:37], v[84:87], v[72:75], v[34:37]
	global_load_dwordx4 v[84:87], v116, s[16:17] offset:3072
	s_waitcnt vmcnt(7)
	v_mfma_f32_16x16x32_f16 v[6:9], v[88:91], v[68:71], v[6:9]
	v_mfma_f32_16x16x32_f16 v[38:41], v[88:91], v[72:75], v[38:41]
	global_load_dwordx4 v[88:91], v116, s[18:19] offset:3072
	s_waitcnt vmcnt(7)
	v_mfma_f32_16x16x32_f16 v[10:13], v[92:95], v[68:71], v[10:13]
	v_mfma_f32_16x16x32_f16 v[42:45], v[92:95], v[72:75], v[42:45]
	global_load_dwordx4 v[92:95], v116, s[20:21] offset:3072
	s_waitcnt vmcnt(7)
	v_mfma_f32_16x16x32_f16 v[14:17], v[96:99], v[68:71], v[14:17]
	v_mfma_f32_16x16x32_f16 v[46:49], v[96:99], v[72:75], v[46:49]
	global_load_dwordx4 v[96:99], v116, s[22:23] offset:3072
	s_waitcnt vmcnt(7)
	v_mfma_f32_16x16x32_f16 v[18:21], v[100:103], v[68:71], v[18:21]
	v_mfma_f32_16x16x32_f16 v[50:53], v[100:103], v[72:75], v[50:53]
	global_load_dwordx4 v[100:103], v116, s[24:25] offset:3072
	s_waitcnt vmcnt(7)
	v_mfma_f32_16x16x32_f16 v[22:25], v[104:107], v[68:71], v[22:25]
	v_mfma_f32_16x16x32_f16 v[54:57], v[104:107], v[72:75], v[54:57]
	global_load_dwordx4 v[104:107], v116, s[26:27] offset:3072
	s_waitcnt vmcnt(7)
	v_mfma_f32_16x16x32_f16 v[26:29], v[108:111], v[68:71], v[26:29]
	v_mfma_f32_16x16x32_f16 v[58:61], v[108:111], v[72:75], v[58:61]
	global_load_dwordx4 v[108:111], v116, s[28:29] offset:3072
	s_waitcnt vmcnt(7)
	v_mfma_f32_16x16x32_f16 v[30:33], v[112:115], v[68:71], v[30:33]
	v_mfma_f32_16x16x32_f16 v[62:65], v[112:115], v[72:75], v[62:65]
	global_load_dwordx4 v[112:115], v116, s[30:31] offset:3072
	s_waitcnt lgkmcnt(0)
	s_waitcnt vmcnt(7)
	v_mfma_f32_16x16x32_f16 v[2:5], v[84:87], v[76:79], v[2:5]
	v_mfma_f32_16x16x32_f16 v[34:37], v[84:87], v[80:83], v[34:37]
	s_waitcnt vmcnt(6)
	v_mfma_f32_16x16x32_f16 v[6:9], v[88:91], v[76:79], v[6:9]
	v_mfma_f32_16x16x32_f16 v[38:41], v[88:91], v[80:83], v[38:41]
	s_waitcnt vmcnt(5)
	v_mfma_f32_16x16x32_f16 v[10:13], v[92:95], v[76:79], v[10:13]
	v_mfma_f32_16x16x32_f16 v[42:45], v[92:95], v[80:83], v[42:45]
	s_waitcnt vmcnt(4)
	v_mfma_f32_16x16x32_f16 v[14:17], v[96:99], v[76:79], v[14:17]
	v_mfma_f32_16x16x32_f16 v[46:49], v[96:99], v[80:83], v[46:49]
	s_waitcnt vmcnt(3)
	v_mfma_f32_16x16x32_f16 v[18:21], v[100:103], v[76:79], v[18:21]
	v_mfma_f32_16x16x32_f16 v[50:53], v[100:103], v[80:83], v[50:53]
	s_waitcnt vmcnt(2)
	v_mfma_f32_16x16x32_f16 v[22:25], v[104:107], v[76:79], v[22:25]
	v_mfma_f32_16x16x32_f16 v[54:57], v[104:107], v[80:83], v[54:57]
	s_waitcnt vmcnt(1)
	v_mfma_f32_16x16x32_f16 v[26:29], v[108:111], v[76:79], v[26:29]
	v_mfma_f32_16x16x32_f16 v[58:61], v[108:111], v[80:83], v[58:61]
	s_waitcnt vmcnt(0)
	v_mfma_f32_16x16x32_f16 v[30:33], v[112:115], v[76:79], v[30:33]
	v_mfma_f32_16x16x32_f16 v[62:65], v[112:115], v[80:83], v[62:65]
	v_cvt_pk_f16_f32 v2, v2, v3
	v_cvt_pk_f16_f32 v3, v4, v5
	v_cvt_pk_f16_f32 v6, v6, v7
	v_cvt_pk_f16_f32 v7, v8, v9
	v_cvt_pk_f16_f32 v10, v10, v11
	v_cvt_pk_f16_f32 v11, v12, v13
	v_cvt_pk_f16_f32 v14, v14, v15
	v_cvt_pk_f16_f32 v15, v16, v17
	v_cvt_pk_f16_f32 v18, v18, v19
	v_cvt_pk_f16_f32 v19, v20, v21
	v_cvt_pk_f16_f32 v22, v22, v23
	v_cvt_pk_f16_f32 v23, v24, v25
	v_cvt_pk_f16_f32 v26, v26, v27
	v_cvt_pk_f16_f32 v27, v28, v29
	v_cvt_pk_f16_f32 v30, v30, v31
	v_cvt_pk_f16_f32 v31, v32, v33
	v_cvt_pk_f16_f32 v34, v34, v35
	v_cvt_pk_f16_f32 v35, v36, v37
	v_cvt_pk_f16_f32 v38, v38, v39
	v_cvt_pk_f16_f32 v39, v40, v41
	v_cvt_pk_f16_f32 v42, v42, v43
	v_cvt_pk_f16_f32 v43, v44, v45
	v_cvt_pk_f16_f32 v46, v46, v47
	v_cvt_pk_f16_f32 v47, v48, v49
	v_cvt_pk_f16_f32 v50, v50, v51
	v_cvt_pk_f16_f32 v51, v52, v53
	v_cvt_pk_f16_f32 v54, v54, v55
	v_cvt_pk_f16_f32 v55, v56, v57
	v_cvt_pk_f16_f32 v58, v58, v59
	v_cvt_pk_f16_f32 v59, v60, v61
	v_cvt_pk_f16_f32 v62, v62, v63
	v_cvt_pk_f16_f32 v63, v64, v65
	ds_write_b64 v120, v[2:3] offset:0
	ds_write_b64 v120, v[6:7] offset:32
	ds_write_b64 v120, v[10:11] offset:64
	ds_write_b64 v120, v[14:15] offset:96
	ds_write_b64 v120, v[18:19] offset:128
	ds_write_b64 v120, v[22:23] offset:160
	ds_write_b64 v120, v[26:27] offset:192
	ds_write_b64 v120, v[30:31] offset:224
	ds_write_b64 v120, v[34:35] offset:4352
	ds_write_b64 v120, v[38:39] offset:4384
	ds_write_b64 v120, v[42:43] offset:4416
	ds_write_b64 v120, v[46:47] offset:4448
	ds_write_b64 v120, v[50:51] offset:4480
	ds_write_b64 v120, v[54:55] offset:4512
	ds_write_b64 v120, v[58:59] offset:4544
	ds_write_b64 v120, v[62:63] offset:4576
	ds_bpermute_b32 v68, v119, v66 offset:0
	ds_bpermute_b32 v69, v119, v66 offset:16
	ds_bpermute_b32 v70, v119, v66 offset:32
	ds_bpermute_b32 v71, v119, v66 offset:48
	ds_bpermute_b32 v72, v119, v66 offset:64
	ds_bpermute_b32 v73, v119, v66 offset:80
	ds_bpermute_b32 v74, v119, v66 offset:96
	ds_bpermute_b32 v75, v119, v66 offset:112
	ds_read_b128 v[84:87], v121 offset:0
	ds_read_b128 v[88:91], v121 offset:1088
	ds_read_b128 v[92:95], v121 offset:2176
	ds_read_b128 v[96:99], v121 offset:3264
	ds_read_b128 v[100:103], v121 offset:4352
	ds_read_b128 v[104:107], v121 offset:5440
	ds_read_b128 v[108:111], v121 offset:6528
	ds_read_b128 v[112:115], v121 offset:7616
	s_waitcnt lgkmcnt(0)
	v_cmp_lt_i32_e64 s[34:35], -1, v68
	v_lshl_add_u32 v76, v68, 8, v67
	s_mov_b64 exec, s[34:35]
	global_store_dwordx4 v76, v[84:87], s[2:3] sc1
	s_mov_b64 exec, -1
	v_cmp_lt_i32_e64 s[34:35], -1, v69
	v_lshl_add_u32 v77, v69, 8, v67
	s_mov_b64 exec, s[34:35]
	global_store_dwordx4 v77, v[88:91], s[2:3] sc1
	s_mov_b64 exec, -1
	v_cmp_lt_i32_e64 s[34:35], -1, v70
	v_lshl_add_u32 v78, v70, 8, v67
	s_mov_b64 exec, s[34:35]
	global_store_dwordx4 v78, v[92:95], s[2:3] sc1
	s_mov_b64 exec, -1
	v_cmp_lt_i32_e64 s[34:35], -1, v71
	v_lshl_add_u32 v79, v71, 8, v67
	s_mov_b64 exec, s[34:35]
	global_store_dwordx4 v79, v[96:99], s[2:3] sc1
	s_mov_b64 exec, -1
	v_cmp_lt_i32_e64 s[34:35], -1, v72
	v_lshl_add_u32 v80, v72, 8, v67
	s_mov_b64 exec, s[34:35]
	global_store_dwordx4 v80, v[100:103], s[2:3]
	s_mov_b64 exec, -1
	v_cmp_lt_i32_e64 s[34:35], -1, v73
	v_lshl_add_u32 v81, v73, 8, v67
	s_mov_b64 exec, s[34:35]
	global_store_dwordx4 v81, v[104:107], s[2:3]
	s_mov_b64 exec, -1
	v_cmp_lt_i32_e64 s[34:35], -1, v74
	v_lshl_add_u32 v82, v74, 8, v67
	s_mov_b64 exec, s[34:35]
	global_store_dwordx4 v82, v[108:111], s[2:3]
	s_mov_b64 exec, -1
	v_cmp_lt_i32_e64 s[34:35], -1, v75
	v_lshl_add_u32 v83, v75, 8, v67
	s_mov_b64 exec, s[34:35]
	global_store_dwordx4 v83, v[112:115], s[2:3]
	s_mov_b64 exec, -1
	s_endpgm
